# tail-fill: MoE-down-0 WGs without a 9th unit convert L1 down experts [56,64) by a hand-written conversion routine; MoE-up-0 conversion WGs do down [0,56)
# baseline (speedup 1.0000x reference)
.LBB0_740:
	s_load_dwordx4 s[0:3], s[8:9], 0x138
	s_waitcnt lgkmcnt(0)
	s_mov_b64 s[4:5], s[0:1]
	s_cmp_lt_i32 s4, 7
	s_cselect_b64 s[0:1], -1, 0
	s_cmp_gt_i32 s5, 6
	s_cselect_b64 s[2:3], -1, 0
	s_and_b64 s[0:1], s[0:1], s[2:3]
	s_andn2_b64 vcc, exec, s[0:1]
	s_cbranch_vccnz .LBB0_960
	s_mov_b64 s[0:1], s[8:9]
	v_mbcnt_lo_u32_b32 v135, -1, 0
	v_mbcnt_hi_u32_b32 v135, -1, v135
	s_load_dword s74, s[8:9], 0x148
	s_add_u32 s2, s8, 0x148
	v_readlane_b32 s4, v243, 0
	s_addc_u32 s3, s9, 0
	v_readlane_b32 s5, v243, 1
	s_waitcnt lgkmcnt(0)
	s_sub_i32 s18, s74, 32
	s_cmp_lt_i32 s4, s18
	s_mov_b64 s[4:5], -1
	s_cbranch_scc1 .LBB0_777
	v_readlane_b32 s4, v243, 0
	s_sub_i32 s4, s4, s18
	s_lshl_b32 s4, s4, 3
	s_add_i32 s19, s4, s94
	s_cmpk_gt_u32 s19, 0x37ff
	v_lshlrev_b32_e32 v141, 1, v135
	v_lshlrev_b32_e32 v140, 2, v135
	v_readlane_b32 s5, v243, 1
	s_cbranch_scc1 .LBB0_753
	s_load_dwordx2 s[4:5], s[0:1], 0x118
	s_load_dwordx2 s[8:9], s[0:1], 0x130
	s_lshl_b32 s6, s19, 14
	s_and_b32 s6, s6, 0x7c00000
	v_and_b32_e32 v132, -16, v141
	s_waitcnt lgkmcnt(0)
	s_add_u32 s10, s4, s6
	s_addc_u32 s11, s5, 0
	s_lshl_b32 s20, s19, 2
	s_and_b32 s6, s20, 0x380
	s_waitcnt vmcnt(0)
	v_add_u32_e32 v0, s6, v132
	v_ashrrev_i32_e32 v1, 31, v0
	v_lshlrev_b64 v[0:1], 12, v[0:1]
	s_lshl_b32 s6, s19, 7
	s_mov_b32 s7, 0
	v_lshl_add_u64 v[0:1], s[10:11], 0, v[0:1]
	s_and_b32 s6, s6, 0xf80
	v_and_b32_e32 v134, 28, v140
	v_lshl_add_u64 v[0:1], v[0:1], 0, s[6:7]
	v_mov_b32_e32 v137, 0
	v_lshlrev_b32_e32 v136, 2, v134
	v_lshl_add_u64 v[64:65], v[0:1], 0, v[136:137]
	s_movk_i32 s21, 0x2000
	v_add_co_u32_e32 v8, vcc, s21, v64
	s_movk_i32 s22, 0x4000
	s_nop 0
	v_addc_co_u32_e32 v9, vcc, 0, v65, vcc
	v_add_co_u32_e32 v16, vcc, s22, v64
	s_movk_i32 s23, 0x6000
	s_nop 0
	v_addc_co_u32_e32 v17, vcc, 0, v65, vcc
	v_add_co_u32_e32 v24, vcc, s23, v64
	s_mov_b32 s24, 0x8000
	s_nop 0
	v_addc_co_u32_e32 v25, vcc, 0, v65, vcc
	v_add_co_u32_e32 v32, vcc, s24, v64
	s_mov_b32 s25, 0xa000
	s_nop 0
	v_addc_co_u32_e32 v33, vcc, 0, v65, vcc
	v_add_co_u32_e32 v40, vcc, s25, v64
	s_mov_b32 s26, 0xc000
	s_nop 0
	v_addc_co_u32_e32 v41, vcc, 0, v65, vcc
	v_add_co_u32_e32 v48, vcc, s26, v64
	s_mov_b32 s6, 0xe000
	s_nop 0
	v_addc_co_u32_e32 v49, vcc, 0, v65, vcc
	v_add_co_u32_e32 v52, vcc, s6, v64
	s_mov_b32 s6, 0xf000
	s_nop 0
	v_addc_co_u32_e32 v53, vcc, 0, v65, vcc
	v_add_co_u32_e32 v66, vcc, s6, v64
	global_load_dwordx4 v[0:3], v[8:9], off offset:-4096 nt
	global_load_dwordx4 v[4:7], v[8:9], off nt
	s_nop 0
	global_load_dwordx4 v[8:11], v[16:17], off offset:-4096 nt
	global_load_dwordx4 v[12:15], v[16:17], off nt
	s_nop 0
	global_load_dwordx4 v[16:19], v[24:25], off offset:-4096 nt
	global_load_dwordx4 v[20:23], v[24:25], off nt
	s_nop 0
	global_load_dwordx4 v[24:27], v[32:33], off offset:-4096 nt
	global_load_dwordx4 v[28:31], v[32:33], off nt
	s_nop 0
	global_load_dwordx4 v[32:35], v[40:41], off offset:-4096 nt
	global_load_dwordx4 v[36:39], v[40:41], off nt
	s_nop 0
	global_load_dwordx4 v[40:43], v[48:49], off offset:-4096 nt
	global_load_dwordx4 v[44:47], v[48:49], off nt
	s_nop 0
	global_load_dwordx4 v[48:51], v[52:53], off offset:-4096 nt
	global_load_dwordx4 v[56:59], v[52:53], off nt
	v_addc_co_u32_e32 v67, vcc, 0, v65, vcc
	global_load_dwordx4 v[52:55], v[64:65], off nt
	global_load_dwordx4 v[60:63], v[66:67], off nt
	s_lshl_b32 s27, s19, 5
	s_add_u32 s29, s8, 0x2900000
	v_readlane_b32 s10, v243, 0
	s_addc_u32 s30, s9, 0
	s_lshl_b32 s6, s10, 3
	s_add_i32 s6, s94, s6
	s_lshl_b32 s10, s74, 3
	s_sub_i32 s6, s6, s10
	s_add_i32 s31, s6, 0x300
	s_lshr_b32 s6, s19, 8
	s_mul_hi_u32 s10, s6, 0x300000
	s_mul_i32 s6, s6, 0x300000
	s_add_u32 s8, s8, s6
	v_ashrrev_i32_e32 v133, 31, v132
	v_lshlrev_b32_e32 v64, 6, v135
	s_addc_u32 s9, s9, s10
	v_and_b32_e32 v142, 0x80, v64
	v_readlane_b32 s11, v243, 1
	v_lshl_add_u64 v[64:65], s[8:9], 0, v[132:133]
	s_mov_b64 s[8:9], 0x2b00c00
	s_mov_b32 s28, 0xb000
	v_lshl_add_u64 v[138:139], v[64:65], 0, s[8:9]
	s_mov_b32 s34, 0xc3e00000
	s_mov_b64 s[8:9], 0x200000
	s_mov_b32 s35, 0x200000
	s_mov_b64 s[10:11], 0x600000
	v_mov_b32_e32 v143, 0x304
	v_mov_b32_e32 v144, 0x43e00000
	s_branch .LBB0_746
.LBB0_744:
	v_mul_f32_e32 v128, 0x42000000, v108
	v_mul_f32_e32 v129, 0x42000000, v68
	v_med3_f32 v131, v128, s34, v144
	v_med3_f32 v129, v129, s34, v144
	v_mov_b32_e32 v128, v137
	v_cvt_pk_fp8_f32 v128, v131, v129
	v_mul_f32_e32 v130, 0x42000000, v64
	v_mul_f32_e32 v129, 0x42000000, v76
	v_med3_f32 v130, v130, s34, v144
	v_med3_f32 v129, v129, s34, v144
	v_cvt_pk_fp8_f32 v128, v130, v129 op_sel:[0,0,1]
	v_mul_f32_e32 v129, 0x42000000, v72
	v_mul_f32_e32 v130, 0x42000000, v84
	v_med3_f32 v145, v129, s34, v144
	v_med3_f32 v130, v130, s34, v144
	v_mov_b32_e32 v129, v137
	v_cvt_pk_fp8_f32 v129, v145, v130
	v_mul_f32_e32 v131, 0x42000000, v80
	v_mul_f32_e32 v130, 0x42000000, v92
	v_med3_f32 v131, v131, s34, v144
	v_med3_f32 v130, v130, s34, v144
	v_cvt_pk_fp8_f32 v129, v131, v130 op_sel:[0,0,1]
	v_mul_f32_e32 v130, 0x42000000, v88
	v_mul_f32_e32 v131, 0x42000000, v100
	v_med3_f32 v148, v130, s34, v144
	v_med3_f32 v131, v131, s34, v144
	v_mov_b32_e32 v130, v137
	v_cvt_pk_fp8_f32 v130, v148, v131
	v_mul_f32_e32 v145, 0x42000000, v96
	v_mul_f32_e32 v131, 0x42000000, v104
	s_lshr_b32 s12, s16, 8
	v_med3_f32 v145, v145, s34, v144
	v_med3_f32 v131, v131, s34, v144
	s_mul_hi_u32 s13, s12, 0x300000
	s_mul_i32 s12, s12, 0x300000
	v_cvt_pk_fp8_f32 v130, v145, v131 op_sel:[0,0,1]
	v_mul_f32_e32 v131, 0x42000000, v112
	v_mul_f32_e32 v145, 0x42000000, v116
	s_add_u32 s12, s29, s12
	v_med3_f32 v149, v131, s34, v144
	v_med3_f32 v145, v145, s34, v144
	v_mov_b32_e32 v131, v137
	s_addc_u32 s13, s30, s13
	v_cvt_pk_fp8_f32 v131, v149, v145
	s_add_u32 s12, s12, s6
	s_addc_u32 s13, s13, 0
	v_mul_f32_e32 v148, 0x42000000, v120
	v_mul_f32_e32 v145, 0x42000000, v124
	v_lshl_add_u64 v[146:147], s[12:13], 0, v[132:133]
	v_med3_f32 v148, v148, s34, v144
	v_med3_f32 v145, v145, s34, v144
	v_cvt_pk_fp8_f32 v131, v148, v145 op_sel:[0,0,1]
	v_lshl_add_u64 v[146:147], v[146:147], 0, v[136:137]
	v_mul_f32_e32 v136, 0x42000000, v109
	v_mul_f32_e32 v145, 0x42000000, v69
	v_lshl_add_u64 v[158:159], v[146:147], 0, s[8:9]
	v_add_co_u32_e32 v160, vcc, s35, v146
	v_med3_f32 v136, v136, s34, v144
	v_med3_f32 v145, v145, s34, v144
	v_mov_b32_e32 v146, v137
	v_cvt_pk_fp8_f32 v146, v136, v145
	v_addc_co_u32_e32 v161, vcc, 0, v147, vcc
	v_mul_f32_e32 v147, 0x42000000, v65
	v_mul_f32_e32 v136, 0x42000000, v77
	v_med3_f32 v145, v147, s34, v144
	v_med3_f32 v136, v136, s34, v144
	v_cvt_pk_fp8_f32 v146, v145, v136 op_sel:[0,0,1]
	v_mul_f32_e32 v136, 0x42000000, v73
	v_mul_f32_e32 v145, 0x42000000, v85
	v_med3_f32 v136, v136, s34, v144
	v_med3_f32 v145, v145, s34, v144
	v_mov_b32_e32 v147, v137
	v_cvt_pk_fp8_f32 v147, v136, v145
	v_mul_f32_e32 v148, 0x42000000, v81
	v_mul_f32_e32 v136, 0x42000000, v93
	v_med3_f32 v145, v148, s34, v144
	v_med3_f32 v136, v136, s34, v144
	v_cvt_pk_fp8_f32 v147, v145, v136 op_sel:[0,0,1]
	v_mul_f32_e32 v136, 0x42000000, v89
	v_mul_f32_e32 v145, 0x42000000, v101
	v_med3_f32 v136, v136, s34, v144
	v_med3_f32 v145, v145, s34, v144
	v_mov_b32_e32 v148, v137
	v_cvt_pk_fp8_f32 v148, v136, v145
	v_mul_f32_e32 v149, 0x42000000, v97
	v_mul_f32_e32 v136, 0x42000000, v105
	v_med3_f32 v145, v149, s34, v144
	v_med3_f32 v136, v136, s34, v144
	v_cvt_pk_fp8_f32 v148, v145, v136 op_sel:[0,0,1]
	v_mul_f32_e32 v136, 0x42000000, v113
	v_mul_f32_e32 v145, 0x42000000, v117
	v_med3_f32 v136, v136, s34, v144
	v_med3_f32 v145, v145, s34, v144
	v_mov_b32_e32 v149, v137
	v_cvt_pk_fp8_f32 v149, v136, v145
	v_mul_f32_e32 v150, 0x42000000, v121
	v_mul_f32_e32 v136, 0x42000000, v125
	v_med3_f32 v145, v150, s34, v144
	v_med3_f32 v136, v136, s34, v144
	v_cvt_pk_fp8_f32 v149, v145, v136 op_sel:[0,0,1]
	v_mul_f32_e32 v136, 0x42000000, v110
	v_mul_f32_e32 v145, 0x42000000, v70
	v_med3_f32 v136, v136, s34, v144
	v_med3_f32 v145, v145, s34, v144
	v_mov_b32_e32 v150, v137
	v_cvt_pk_fp8_f32 v150, v136, v145
	v_mul_f32_e32 v151, 0x42000000, v66
	v_mul_f32_e32 v136, 0x42000000, v78
	v_med3_f32 v145, v151, s34, v144
	v_med3_f32 v136, v136, s34, v144
	v_cvt_pk_fp8_f32 v150, v145, v136 op_sel:[0,0,1]
	v_mul_f32_e32 v136, 0x42000000, v74
	v_mul_f32_e32 v145, 0x42000000, v86
	v_med3_f32 v136, v136, s34, v144
	v_med3_f32 v145, v145, s34, v144
	v_mov_b32_e32 v151, v137
	v_cvt_pk_fp8_f32 v151, v136, v145
	v_mul_f32_e32 v152, 0x42000000, v82
	v_mul_f32_e32 v136, 0x42000000, v94
	v_med3_f32 v145, v152, s34, v144
	v_med3_f32 v136, v136, s34, v144
	v_cvt_pk_fp8_f32 v151, v145, v136 op_sel:[0,0,1]
	v_mul_f32_e32 v136, 0x42000000, v90
	v_mul_f32_e32 v145, 0x42000000, v102
	v_med3_f32 v136, v136, s34, v144
	v_med3_f32 v145, v145, s34, v144
	v_mov_b32_e32 v152, v137
	v_cvt_pk_fp8_f32 v152, v136, v145
	v_mul_f32_e32 v153, 0x42000000, v98
	v_mul_f32_e32 v136, 0x42000000, v106
	v_med3_f32 v145, v153, s34, v144
	v_med3_f32 v136, v136, s34, v144
	v_cvt_pk_fp8_f32 v152, v145, v136 op_sel:[0,0,1]
	v_mul_f32_e32 v136, 0x42000000, v114
	v_mul_f32_e32 v145, 0x42000000, v118
	v_med3_f32 v136, v136, s34, v144
	v_med3_f32 v145, v145, s34, v144
	v_mov_b32_e32 v153, v137
	v_cvt_pk_fp8_f32 v153, v136, v145
	v_mul_f32_e32 v154, 0x42000000, v122
	v_mul_f32_e32 v136, 0x42000000, v126
	v_med3_f32 v145, v154, s34, v144
	v_med3_f32 v136, v136, s34, v144
	v_cvt_pk_fp8_f32 v153, v145, v136 op_sel:[0,0,1]
	v_mul_f32_e32 v136, 0x42000000, v111
	v_mul_f32_e32 v145, 0x42000000, v71
	v_med3_f32 v136, v136, s34, v144
	v_med3_f32 v145, v145, s34, v144
	v_mov_b32_e32 v154, v137
	v_cvt_pk_fp8_f32 v154, v136, v145
	v_mul_f32_e32 v155, 0x42000000, v67
	v_mul_f32_e32 v136, 0x42000000, v79
	v_med3_f32 v145, v155, s34, v144
	v_med3_f32 v136, v136, s34, v144
	v_cvt_pk_fp8_f32 v154, v145, v136 op_sel:[0,0,1]
	v_mul_f32_e32 v136, 0x42000000, v75
	v_mul_f32_e32 v145, 0x42000000, v87
	v_med3_f32 v136, v136, s34, v144
	v_med3_f32 v145, v145, s34, v144
	v_mov_b32_e32 v155, v137
	v_cvt_pk_fp8_f32 v155, v136, v145
	v_mul_f32_e32 v156, 0x42000000, v83
	v_mul_f32_e32 v136, 0x42000000, v95
	v_med3_f32 v145, v156, s34, v144
	v_med3_f32 v136, v136, s34, v144
	v_cvt_pk_fp8_f32 v155, v145, v136 op_sel:[0,0,1]
	v_mul_f32_e32 v136, 0x42000000, v91
	v_mul_f32_e32 v145, 0x42000000, v103
	v_med3_f32 v136, v136, s34, v144
	v_med3_f32 v145, v145, s34, v144
	v_mov_b32_e32 v156, v137
	v_cvt_pk_fp8_f32 v156, v136, v145
	v_mul_f32_e32 v157, 0x42000000, v99
	v_mul_f32_e32 v136, 0x42000000, v107
	v_med3_f32 v145, v157, s34, v144
	v_med3_f32 v136, v136, s34, v144
	v_cvt_pk_fp8_f32 v156, v145, v136 op_sel:[0,0,1]
	v_mul_f32_e32 v136, 0x42000000, v115
	v_mul_f32_e32 v145, 0x42000000, v119
	v_med3_f32 v136, v136, s34, v144
	v_med3_f32 v145, v145, s34, v144
	v_mov_b32_e32 v157, v137
	v_cvt_pk_fp8_f32 v157, v136, v145
	v_mul_f32_e32 v162, 0x42000000, v123
	v_mul_f32_e32 v136, 0x42000000, v127
	s_addk_i32 s31, 0x200
	s_addk_i32 s20, 0x800
	s_addk_i32 s27, 0x4000
	v_med3_f32 v145, v162, s34, v144
	v_med3_f32 v136, v136, s34, v144
	s_cmpk_gt_i32 s36, 0x35ff
	v_cvt_pk_fp8_f32 v157, v145, v136 op_sel:[0,0,1]
	v_lshl_add_u64 v[138:139], v[138:139], 0, s[10:11]
	s_cselect_b64 s[14:15], -1, 0
	global_store_dwordx4 v[160:161], v[128:131], off
	global_store_dwordx4 v[158:159], v[146:149], off offset:1024
	global_store_dwordx4 v[158:159], v[150:153], off offset:2048
	global_store_dwordx4 v[158:159], v[154:157], off offset:3072

.LBB0_746:
	s_add_i32 s36, s31, 0xfffffe00
	s_cmpk_lt_i32 s36, 0x3700
	s_cselect_b64 s[14:15], -1, 0
	s_mov_b64 s[16:17], -1
	s_and_b64 vcc, exec, s[14:15]
	s_cbranch_vccnz .LBB0_748
	s_and_b32 s6, s20, 0x380
	s_and_b32 s12, s27, 0x3e0
	s_mov_b64 s[16:17], 0

.LBB0_750:
	v_or_b32_e32 v128, s12, v134
	v_lshrrev_b32_e32 v128, 1, v128
	v_and_b32_e32 v128, 0x78, v128
	v_bitop3_b32 v129, s12, v143, v134 bitop3:0xc8
	v_or3_b32 v136, v142, v129, v128
	s_waitcnt vmcnt(1)
	v_mul_f32_e32 v128, 0x42000000, v52
	v_mul_f32_e32 v129, 0x42000000, v0
	v_med3_f32 v131, v128, s34, v144
	v_med3_f32 v129, v129, s34, v144
	v_mov_b32_e32 v128, v137
	v_cvt_pk_fp8_f32 v128, v131, v129
	v_mul_f32_e32 v130, 0x42000000, v4
	v_mul_f32_e32 v129, 0x42000000, v8
	v_med3_f32 v130, v130, s34, v144
	v_med3_f32 v129, v129, s34, v144
	v_cvt_pk_fp8_f32 v128, v130, v129 op_sel:[0,0,1]
	v_mul_f32_e32 v129, 0x42000000, v12
	v_mul_f32_e32 v130, 0x42000000, v16
	v_med3_f32 v145, v129, s34, v144
	v_med3_f32 v130, v130, s34, v144
	v_mov_b32_e32 v129, v137
	v_cvt_pk_fp8_f32 v129, v145, v130
	v_mul_f32_e32 v131, 0x42000000, v20
	v_mul_f32_e32 v130, 0x42000000, v24
	v_med3_f32 v131, v131, s34, v144
	v_med3_f32 v130, v130, s34, v144
	v_cvt_pk_fp8_f32 v129, v131, v130 op_sel:[0,0,1]
	v_mul_f32_e32 v130, 0x42000000, v28
	v_mul_f32_e32 v131, 0x42000000, v32
	v_med3_f32 v146, v130, s34, v144
	v_med3_f32 v131, v131, s34, v144
	v_mov_b32_e32 v130, v137
	v_cvt_pk_fp8_f32 v130, v146, v131
	v_mul_f32_e32 v145, 0x42000000, v36
	v_mul_f32_e32 v131, 0x42000000, v40
	v_med3_f32 v145, v145, s34, v144
	v_med3_f32 v131, v131, s34, v144
	v_cvt_pk_fp8_f32 v130, v145, v131 op_sel:[0,0,1]
	v_mul_f32_e32 v131, 0x42000000, v44
	v_mul_f32_e32 v145, 0x42000000, v48
	v_med3_f32 v147, v131, s34, v144
	v_med3_f32 v145, v145, s34, v144
	v_mov_b32_e32 v131, v137
	v_cvt_pk_fp8_f32 v131, v147, v145
	v_mul_f32_e32 v146, 0x42000000, v56
	s_waitcnt vmcnt(0)
	v_mul_f32_e32 v145, 0x42000000, v60
	v_med3_f32 v146, v146, s34, v144
	v_med3_f32 v145, v145, s34, v144
	v_lshlrev_b32_e32 v136, 10, v136
	v_cvt_pk_fp8_f32 v131, v146, v145 op_sel:[0,0,1]
	v_lshl_add_u64 v[146:147], v[136:137], 0, s[6:7]
	v_lshl_add_u64 v[158:159], v[138:139], 0, v[146:147]
	v_mul_f32_e32 v145, 0x42000000, v53
	v_mul_f32_e32 v146, 0x42000000, v1
	v_med3_f32 v145, v145, s34, v144
	v_med3_f32 v148, v146, s34, v144
	v_mov_b32_e32 v146, v137
	v_cvt_pk_fp8_f32 v146, v145, v148
	v_mul_f32_e32 v147, 0x42000000, v5
	v_mul_f32_e32 v145, 0x42000000, v9
	v_med3_f32 v147, v147, s34, v144
	v_med3_f32 v145, v145, s34, v144
	v_cvt_pk_fp8_f32 v146, v147, v145 op_sel:[0,0,1]
	v_mul_f32_e32 v145, 0x42000000, v13
	v_mul_f32_e32 v147, 0x42000000, v17
	v_med3_f32 v145, v145, s34, v144
	v_med3_f32 v149, v147, s34, v144
	v_mov_b32_e32 v147, v137
	v_cvt_pk_fp8_f32 v147, v145, v149
	v_mul_f32_e32 v148, 0x42000000, v21
	v_mul_f32_e32 v145, 0x42000000, v25
	v_med3_f32 v148, v148, s34, v144
	v_med3_f32 v145, v145, s34, v144
	v_cvt_pk_fp8_f32 v147, v148, v145 op_sel:[0,0,1]
	v_mul_f32_e32 v145, 0x42000000, v29
	v_mul_f32_e32 v148, 0x42000000, v33
	v_med3_f32 v145, v145, s34, v144
	v_med3_f32 v150, v148, s34, v144
	v_mov_b32_e32 v148, v137
	v_cvt_pk_fp8_f32 v148, v145, v150
	v_mul_f32_e32 v149, 0x42000000, v37
	v_mul_f32_e32 v145, 0x42000000, v41
	v_med3_f32 v149, v149, s34, v144
	v_med3_f32 v145, v145, s34, v144
	v_cvt_pk_fp8_f32 v148, v149, v145 op_sel:[0,0,1]
	v_mul_f32_e32 v145, 0x42000000, v45
	v_mul_f32_e32 v149, 0x42000000, v49
	v_med3_f32 v145, v145, s34, v144
	v_med3_f32 v151, v149, s34, v144
	v_mov_b32_e32 v149, v137
	v_cvt_pk_fp8_f32 v149, v145, v151
	v_mul_f32_e32 v150, 0x42000000, v57
	v_mul_f32_e32 v145, 0x42000000, v61
	v_med3_f32 v150, v150, s34, v144
	v_med3_f32 v145, v145, s34, v144
	v_cvt_pk_fp8_f32 v149, v150, v145 op_sel:[0,0,1]
	v_mul_f32_e32 v145, 0x42000000, v54
	v_mul_f32_e32 v150, 0x42000000, v2
	v_med3_f32 v145, v145, s34, v144
	v_med3_f32 v152, v150, s34, v144
	v_mov_b32_e32 v150, v137
	v_cvt_pk_fp8_f32 v150, v145, v152
	v_mul_f32_e32 v151, 0x42000000, v6
	v_mul_f32_e32 v145, 0x42000000, v10
	v_med3_f32 v151, v151, s34, v144
	v_med3_f32 v145, v145, s34, v144
	v_cvt_pk_fp8_f32 v150, v151, v145 op_sel:[0,0,1]
	v_mul_f32_e32 v145, 0x42000000, v14
	v_mul_f32_e32 v151, 0x42000000, v18
	v_med3_f32 v145, v145, s34, v144
	v_med3_f32 v153, v151, s34, v144
	v_mov_b32_e32 v151, v137
	v_cvt_pk_fp8_f32 v151, v145, v153
	v_mul_f32_e32 v152, 0x42000000, v22
	v_mul_f32_e32 v145, 0x42000000, v26
	v_med3_f32 v152, v152, s34, v144
	v_med3_f32 v145, v145, s34, v144
	v_cvt_pk_fp8_f32 v151, v152, v145 op_sel:[0,0,1]
	v_mul_f32_e32 v145, 0x42000000, v30
	v_mul_f32_e32 v152, 0x42000000, v34
	v_med3_f32 v145, v145, s34, v144
	v_med3_f32 v154, v152, s34, v144
	v_mov_b32_e32 v152, v137
	v_cvt_pk_fp8_f32 v152, v145, v154
	v_mul_f32_e32 v153, 0x42000000, v38
	v_mul_f32_e32 v145, 0x42000000, v42
	v_med3_f32 v153, v153, s34, v144
	v_med3_f32 v145, v145, s34, v144
	v_cvt_pk_fp8_f32 v152, v153, v145 op_sel:[0,0,1]
	v_mul_f32_e32 v145, 0x42000000, v46
	v_mul_f32_e32 v153, 0x42000000, v50
	v_med3_f32 v145, v145, s34, v144
	v_med3_f32 v155, v153, s34, v144
	v_mov_b32_e32 v153, v137
	v_cvt_pk_fp8_f32 v153, v145, v155
	v_mul_f32_e32 v154, 0x42000000, v58
	v_mul_f32_e32 v145, 0x42000000, v62
	v_med3_f32 v154, v154, s34, v144
	v_med3_f32 v145, v145, s34, v144
	v_cvt_pk_fp8_f32 v153, v154, v145 op_sel:[0,0,1]
	v_mul_f32_e32 v145, 0x42000000, v55
	v_mul_f32_e32 v154, 0x42000000, v3
	v_med3_f32 v145, v145, s34, v144
	v_med3_f32 v156, v154, s34, v144
	v_mov_b32_e32 v154, v137
	v_cvt_pk_fp8_f32 v154, v145, v156
	v_mul_f32_e32 v155, 0x42000000, v7
	v_mul_f32_e32 v145, 0x42000000, v11
	v_med3_f32 v155, v155, s34, v144
	v_med3_f32 v145, v145, s34, v144
	v_cvt_pk_fp8_f32 v154, v155, v145 op_sel:[0,0,1]
	v_mul_f32_e32 v145, 0x42000000, v15
	v_mul_f32_e32 v155, 0x42000000, v19
	v_med3_f32 v145, v145, s34, v144
	v_med3_f32 v157, v155, s34, v144
	v_mov_b32_e32 v155, v137
	v_cvt_pk_fp8_f32 v155, v145, v157
	v_mul_f32_e32 v156, 0x42000000, v23
	v_mul_f32_e32 v145, 0x42000000, v27
	v_med3_f32 v156, v156, s34, v144
	v_med3_f32 v145, v145, s34, v144
	v_cvt_pk_fp8_f32 v155, v156, v145 op_sel:[0,0,1]
	v_mul_f32_e32 v145, 0x42000000, v31
	v_mul_f32_e32 v156, 0x42000000, v35
	v_med3_f32 v145, v145, s34, v144
	v_med3_f32 v160, v156, s34, v144
	v_mov_b32_e32 v156, v137
	v_cvt_pk_fp8_f32 v156, v145, v160
	v_mul_f32_e32 v157, 0x42000000, v39
	v_mul_f32_e32 v145, 0x42000000, v43
	v_med3_f32 v157, v157, s34, v144
	v_med3_f32 v145, v145, s34, v144
	v_cvt_pk_fp8_f32 v156, v157, v145 op_sel:[0,0,1]
	v_mul_f32_e32 v145, 0x42000000, v47
	v_mul_f32_e32 v157, 0x42000000, v51
	v_med3_f32 v145, v145, s34, v144
	v_med3_f32 v161, v157, s34, v144
	v_mov_b32_e32 v157, v137
	v_cvt_pk_fp8_f32 v157, v145, v161
	v_mul_f32_e32 v160, 0x42000000, v59
	v_mul_f32_e32 v145, 0x42000000, v63
	v_med3_f32 v160, v160, s34, v144
	v_med3_f32 v145, v145, s34, v144
	v_cvt_pk_fp8_f32 v157, v160, v145 op_sel:[0,0,1]
	s_andn2_b64 vcc, exec, s[14:15]
	s_mov_b64 s[14:15], -1
	global_store_dwordx4 v[158:159], v[128:131], off offset:-3072
	global_store_dwordx4 v[158:159], v[146:149], off offset:-2048
	global_store_dwordx4 v[158:159], v[150:153], off offset:-1024
	global_store_dwordx4 v[158:159], v[154:157], off
	s_cbranch_vccnz .LBB0_745
	s_cmpk_gt_i32 s36, 0x35ff
	s_cbranch_scc1 .LBB0_744
	s_lshr_b32 s14, s31, 8
	s_mov_b32 s15, s7
	s_lshl_b64 s[14:15], s[14:15], 22
	v_add_u32_e32 v0, s6, v132
	s_add_u32 s14, s4, s14
	v_ashrrev_i32_e32 v1, 31, v0
	s_addc_u32 s15, s5, s15
	v_lshlrev_b64 v[0:1], 12, v[0:1]
	v_lshl_add_u64 v[0:1], s[14:15], 0, v[0:1]
	s_mov_b32 s13, s7
	v_lshl_add_u64 v[0:1], s[12:13], 2, v[0:1]
	v_lshlrev_b32_e32 v2, 2, v134
	v_mov_b32_e32 v3, v137
	v_lshl_add_u64 v[56:57], v[0:1], 0, v[2:3]
	v_add_co_u32_e32 v8, vcc, s21, v56
	s_nop 1
	v_addc_co_u32_e32 v9, vcc, 0, v57, vcc
	v_add_co_u32_e32 v16, vcc, s22, v56
	global_load_dwordx4 v[0:3], v[8:9], off offset:-4096 nt
	global_load_dwordx4 v[4:7], v[8:9], off nt
	v_addc_co_u32_e32 v17, vcc, 0, v57, vcc
	v_add_co_u32_e32 v24, vcc, s23, v56
	global_load_dwordx4 v[8:11], v[16:17], off offset:-4096 nt
	global_load_dwordx4 v[12:15], v[16:17], off nt
	v_addc_co_u32_e32 v25, vcc, 0, v57, vcc
	v_add_co_u32_e32 v32, vcc, s24, v56
	global_load_dwordx4 v[16:19], v[24:25], off offset:-4096 nt
	global_load_dwordx4 v[20:23], v[24:25], off nt
	v_addc_co_u32_e32 v33, vcc, 0, v57, vcc
	v_add_co_u32_e32 v40, vcc, s25, v56
	global_load_dwordx4 v[24:27], v[32:33], off offset:-4096 nt
	global_load_dwordx4 v[28:31], v[32:33], off nt
	v_addc_co_u32_e32 v41, vcc, 0, v57, vcc
	v_add_co_u32_e32 v44, vcc, s26, v56
	global_load_dwordx4 v[32:35], v[40:41], off offset:-4096 nt
	global_load_dwordx4 v[36:39], v[40:41], off nt
	v_addc_co_u32_e32 v45, vcc, 0, v57, vcc
	v_add_co_u32_e32 v48, vcc, 0xd000, v56
	global_load_dwordx4 v[40:43], v[44:45], off offset:-4096 nt
	s_nop 0
	global_load_dwordx4 v[44:47], v[44:45], off nt
	v_addc_co_u32_e32 v49, vcc, 0, v57, vcc
	v_add_co_u32_e32 v58, vcc, 0xe000, v56
	global_load_dwordx4 v[52:55], v[56:57], off nt
	s_nop 0
	global_load_dwordx4 v[48:51], v[48:49], off nt
	v_addc_co_u32_e32 v59, vcc, 0, v57, vcc
	v_add_co_u32_e32 v60, vcc, 0xf000, v56
	s_nop 1
	v_addc_co_u32_e32 v61, vcc, 0, v57, vcc
	global_load_dwordx4 v[56:59], v[58:59], off nt
	s_nop 0
	global_load_dwordx4 v[60:63], v[60:61], off nt
	s_branch .LBB0_744

.LBB0_1116:
	v_readlane_b32 s4, v243, 0
	v_mov_b32_e32 v0, 0x20184
	ds_read_b32 v0, v0
	s_waitcnt lgkmcnt(0)
	v_readfirstlane_b32 s5, v0
	s_lshl_b32 s5, s5, 2
	s_sub_i32 s5, s5, 0x800
	s_max_i32 s5, s5, 0
	s_min_i32 s5, s5, 192
	s_cmp_lt_i32 s4, s5
	s_cbranch_scc1 .Ltf7_done
	s_sub_i32 s4, s4, s5
	s_lshl_b32 s4, s4, 3
	s_lshr_b32 s6, s33, 6
	s_add_i32 s4, s4, s6
	s_sub_i32 s5, 0x100, s5
	s_lshl_b32 s5, s5, 3
	s_movk_i32 s6, 0x800
	s_waitcnt vmcnt(0)
	s_cmp_ge_u32 s4, s6
	s_cbranch_scc1 .Ltf7_done
	v_readlane_b32 s8, v243, 7
	v_readlane_b32 s9, v243, 8
	s_load_dwordx2 s[10:11], s[8:9], 0x130
	s_load_dwordx2 s[12:13], s[8:9], 0x118
	v_mbcnt_lo_u32_b32 v163, -1, 0
	v_mbcnt_hi_u32_b32 v163, -1, v163
	v_lshrrev_b32_e32 v164, 3, v163
	v_and_b32_e32 v163, 7, v163
	v_lshlrev_b32_e32 v144, 16, v164
	v_lshl_add_u32 v144, v163, 4, v144
	v_add_u32_e32 v145, 0x1000, v144
	v_add_u32_e32 v146, 0x2000, v144
	v_add_u32_e32 v147, 0x3000, v144
	v_add_u32_e32 v148, 0x4000, v144
	v_add_u32_e32 v149, 0x5000, v144
	v_add_u32_e32 v150, 0x6000, v144
	v_add_u32_e32 v151, 0x7000, v144
	v_add_u32_e32 v152, 0x8000, v144
	v_add_u32_e32 v153, 0x9000, v144
	v_add_u32_e32 v154, 0xa000, v144
	v_add_u32_e32 v155, 0xb000, v144
	v_add_u32_e32 v156, 0xc000, v144
	v_add_u32_e32 v157, 0xd000, v144
	v_add_u32_e32 v158, 0xe000, v144
	v_add_u32_e32 v159, 0xf000, v144
	v_bfe_u32 v161, v163, 1, 1
	v_lshlrev_b32_e32 v161, 17, v161
	v_lshrrev_b32_e32 v165, 2, v163
	v_lshl_add_u32 v161, v165, 13, v161
	v_and_b32_e32 v165, 1, v163
	v_lshl_add_u32 v161, v165, 12, v161
	v_lshl_add_u32 v161, v164, 4, v161
	v_mov_b32_e32 v162, 0x43e00000
	s_mov_b32 s28, 0xc3e00000
	s_waitcnt lgkmcnt(0)
	s_add_u32 s10, s10, 0x2b00000
	s_addc_u32 s11, s11, 0
	s_lshr_b32 s22, s4, 8
	s_and_b32 s23, s4, 0xff
	s_mov_b64 s[16:17], s[12:13]
	s_add_i32 s22, s22, 56
	s_lshl_b32 s24, s22, 22
	s_lshr_b32 s25, s23, 5
	s_lshl_b32 s25, s25, 19
	s_and_b32 s26, s23, 31
	s_lshl_b32 s26, s26, 7
	s_add_i32 s24, s24, s25
	s_add_i32 s24, s24, s26
	s_add_u32 s16, s16, s24
	s_addc_u32 s17, s17, 0
	s_nop 0
	global_load_dwordx4 v[0:3], v144, s[16:17] nt
	global_load_dwordx4 v[4:7], v145, s[16:17] nt
	global_load_dwordx4 v[8:11], v146, s[16:17] nt
	global_load_dwordx4 v[12:15], v147, s[16:17] nt
	global_load_dwordx4 v[16:19], v148, s[16:17] nt
	global_load_dwordx4 v[20:23], v149, s[16:17] nt
	global_load_dwordx4 v[24:27], v150, s[16:17] nt
	global_load_dwordx4 v[28:31], v151, s[16:17] nt
	global_load_dwordx4 v[32:35], v152, s[16:17] nt
	global_load_dwordx4 v[36:39], v153, s[16:17] nt
	global_load_dwordx4 v[40:43], v154, s[16:17] nt
	global_load_dwordx4 v[44:47], v155, s[16:17] nt
	global_load_dwordx4 v[48:51], v156, s[16:17] nt
	global_load_dwordx4 v[52:55], v157, s[16:17] nt
	global_load_dwordx4 v[56:59], v158, s[16:17] nt
	global_load_dwordx4 v[60:63], v159, s[16:17] nt
	s_add_i32 s7, s4, s5
	s_cmp_lt_u32 s7, s6
	s_cbranch_scc0 .Ltf7_p_last
	s_lshr_b32 s22, s7, 8
	s_and_b32 s23, s7, 0xff
	s_mov_b64 s[16:17], s[12:13]
	s_add_i32 s22, s22, 56
	s_lshl_b32 s24, s22, 22
	s_lshr_b32 s25, s23, 5
	s_lshl_b32 s25, s25, 19
	s_and_b32 s26, s23, 31
	s_lshl_b32 s26, s26, 7
	s_add_i32 s24, s24, s25
	s_add_i32 s24, s24, s26
	s_add_u32 s16, s16, s24
	s_addc_u32 s17, s17, 0
	s_nop 0
	global_load_dwordx4 v[64:67], v144, s[16:17] nt
	global_load_dwordx4 v[68:71], v145, s[16:17] nt
	global_load_dwordx4 v[72:75], v146, s[16:17] nt
	global_load_dwordx4 v[76:79], v147, s[16:17] nt
	global_load_dwordx4 v[80:83], v148, s[16:17] nt
	global_load_dwordx4 v[84:87], v149, s[16:17] nt
	global_load_dwordx4 v[88:91], v150, s[16:17] nt
	global_load_dwordx4 v[92:95], v151, s[16:17] nt
	global_load_dwordx4 v[96:99], v152, s[16:17] nt
	global_load_dwordx4 v[100:103], v153, s[16:17] nt
	global_load_dwordx4 v[104:107], v154, s[16:17] nt
	global_load_dwordx4 v[108:111], v155, s[16:17] nt
	global_load_dwordx4 v[112:115], v156, s[16:17] nt
	global_load_dwordx4 v[116:119], v157, s[16:17] nt
	global_load_dwordx4 v[120:123], v158, s[16:17] nt
	global_load_dwordx4 v[124:127], v159, s[16:17] nt
	s_waitcnt vmcnt(16)
	s_branch .Ltf7_p_st

.Ltf7_p_st:
	s_lshr_b32 s22, s4, 8
	s_and_b32 s23, s4, 0xff
	s_add_i32 s22, s22, 56
	s_mul_i32 s24, s22, 0x300000
	s_lshr_b32 s25, s23, 5
	s_lshl_b32 s25, s25, 7
	s_add_i32 s24, s24, s25
	s_and_b32 s26, s23, 31
	s_lshr_b32 s25, s26, 3
	s_lshl_b32 s25, s25, 18
	s_add_i32 s24, s24, s25
	s_bfe_u32 s25, s26, 0x20001
	s_lshl_b32 s25, s25, 15
	s_add_i32 s24, s24, s25
	s_and_b32 s25, s26, 1
	s_lshl_b32 s25, s25, 14
	s_add_i32 s24, s24, s25
	s_add_u32 s20, s10, s24
	s_addc_u32 s21, s11, 0
	v_mul_f32_e32 v0, 0x42000000, v0
	v_mul_f32_e32 v4, 0x42000000, v4
	v_mul_f32_e32 v8, 0x42000000, v8
	v_mul_f32_e32 v12, 0x42000000, v12
	v_mul_f32_e32 v16, 0x42000000, v16
	v_mul_f32_e32 v20, 0x42000000, v20
	v_mul_f32_e32 v24, 0x42000000, v24
	v_mul_f32_e32 v28, 0x42000000, v28
	v_mul_f32_e32 v32, 0x42000000, v32
	v_mul_f32_e32 v36, 0x42000000, v36
	v_mul_f32_e32 v40, 0x42000000, v40
	v_mul_f32_e32 v44, 0x42000000, v44
	v_mul_f32_e32 v48, 0x42000000, v48
	v_mul_f32_e32 v52, 0x42000000, v52
	v_mul_f32_e32 v56, 0x42000000, v56
	v_mul_f32_e32 v60, 0x42000000, v60
	v_med3_f32 v0, v0, s28, v162
	v_med3_f32 v4, v4, s28, v162
	v_med3_f32 v8, v8, s28, v162
	v_med3_f32 v12, v12, s28, v162
	v_med3_f32 v16, v16, s28, v162
	v_med3_f32 v20, v20, s28, v162
	v_med3_f32 v24, v24, s28, v162
	v_med3_f32 v28, v28, s28, v162
	v_med3_f32 v32, v32, s28, v162
	v_med3_f32 v36, v36, s28, v162
	v_med3_f32 v40, v40, s28, v162
	v_med3_f32 v44, v44, s28, v162
	v_med3_f32 v48, v48, s28, v162
	v_med3_f32 v52, v52, s28, v162
	v_med3_f32 v56, v56, s28, v162
	v_med3_f32 v60, v60, s28, v162
	v_cvt_pk_fp8_f32 v128, v0, v4
	v_cvt_pk_fp8_f32 v129, v16, v20
	v_cvt_pk_fp8_f32 v130, v32, v36
	v_cvt_pk_fp8_f32 v131, v48, v52
	v_cvt_pk_fp8_f32 v128, v8, v12 op_sel:[0,0,1]
	v_cvt_pk_fp8_f32 v129, v24, v28 op_sel:[0,0,1]
	v_cvt_pk_fp8_f32 v130, v40, v44 op_sel:[0,0,1]
	v_cvt_pk_fp8_f32 v131, v56, v60 op_sel:[0,0,1]
	s_nop 0
	global_store_dwordx4 v161, v[128:131], s[20:21]
	v_mul_f32_e32 v1, 0x42000000, v1
	v_mul_f32_e32 v5, 0x42000000, v5
	v_mul_f32_e32 v9, 0x42000000, v9
	v_mul_f32_e32 v13, 0x42000000, v13
	v_mul_f32_e32 v17, 0x42000000, v17
	v_mul_f32_e32 v21, 0x42000000, v21
	v_mul_f32_e32 v25, 0x42000000, v25
	v_mul_f32_e32 v29, 0x42000000, v29
	v_mul_f32_e32 v33, 0x42000000, v33
	v_mul_f32_e32 v37, 0x42000000, v37
	v_mul_f32_e32 v41, 0x42000000, v41
	v_mul_f32_e32 v45, 0x42000000, v45
	v_mul_f32_e32 v49, 0x42000000, v49
	v_mul_f32_e32 v53, 0x42000000, v53
	v_mul_f32_e32 v57, 0x42000000, v57
	v_mul_f32_e32 v61, 0x42000000, v61
	v_med3_f32 v1, v1, s28, v162
	v_med3_f32 v5, v5, s28, v162
	v_med3_f32 v9, v9, s28, v162
	v_med3_f32 v13, v13, s28, v162
	v_med3_f32 v17, v17, s28, v162
	v_med3_f32 v21, v21, s28, v162
	v_med3_f32 v25, v25, s28, v162
	v_med3_f32 v29, v29, s28, v162
	v_med3_f32 v33, v33, s28, v162
	v_med3_f32 v37, v37, s28, v162
	v_med3_f32 v41, v41, s28, v162
	v_med3_f32 v45, v45, s28, v162
	v_med3_f32 v49, v49, s28, v162
	v_med3_f32 v53, v53, s28, v162
	v_med3_f32 v57, v57, s28, v162
	v_med3_f32 v61, v61, s28, v162
	v_cvt_pk_fp8_f32 v136, v1, v5
	v_cvt_pk_fp8_f32 v137, v17, v21
	v_cvt_pk_fp8_f32 v138, v33, v37
	v_cvt_pk_fp8_f32 v139, v49, v53
	v_cvt_pk_fp8_f32 v136, v9, v13 op_sel:[0,0,1]
	v_cvt_pk_fp8_f32 v137, v25, v29 op_sel:[0,0,1]
	v_cvt_pk_fp8_f32 v138, v41, v45 op_sel:[0,0,1]
	v_cvt_pk_fp8_f32 v139, v57, v61 op_sel:[0,0,1]
	s_nop 0
	global_store_dwordx4 v161, v[136:139], s[20:21] offset:1024
	v_mul_f32_e32 v2, 0x42000000, v2
	v_mul_f32_e32 v6, 0x42000000, v6
	v_mul_f32_e32 v10, 0x42000000, v10
	v_mul_f32_e32 v14, 0x42000000, v14
	v_mul_f32_e32 v18, 0x42000000, v18
	v_mul_f32_e32 v22, 0x42000000, v22
	v_mul_f32_e32 v26, 0x42000000, v26
	v_mul_f32_e32 v30, 0x42000000, v30
	v_mul_f32_e32 v34, 0x42000000, v34
	v_mul_f32_e32 v38, 0x42000000, v38
	v_mul_f32_e32 v42, 0x42000000, v42
	v_mul_f32_e32 v46, 0x42000000, v46
	v_mul_f32_e32 v50, 0x42000000, v50
	v_mul_f32_e32 v54, 0x42000000, v54
	v_mul_f32_e32 v58, 0x42000000, v58
	v_mul_f32_e32 v62, 0x42000000, v62
	v_med3_f32 v2, v2, s28, v162
	v_med3_f32 v6, v6, s28, v162
	v_med3_f32 v10, v10, s28, v162
	v_med3_f32 v14, v14, s28, v162
	v_med3_f32 v18, v18, s28, v162
	v_med3_f32 v22, v22, s28, v162
	v_med3_f32 v26, v26, s28, v162
	v_med3_f32 v30, v30, s28, v162
	v_med3_f32 v34, v34, s28, v162
	v_med3_f32 v38, v38, s28, v162
	v_med3_f32 v42, v42, s28, v162
	v_med3_f32 v46, v46, s28, v162
	v_med3_f32 v50, v50, s28, v162
	v_med3_f32 v54, v54, s28, v162
	v_med3_f32 v58, v58, s28, v162
	v_med3_f32 v62, v62, s28, v162
	v_cvt_pk_fp8_f32 v128, v2, v6
	v_cvt_pk_fp8_f32 v129, v18, v22
	v_cvt_pk_fp8_f32 v130, v34, v38
	v_cvt_pk_fp8_f32 v131, v50, v54
	v_cvt_pk_fp8_f32 v128, v10, v14 op_sel:[0,0,1]
	v_cvt_pk_fp8_f32 v129, v26, v30 op_sel:[0,0,1]
	v_cvt_pk_fp8_f32 v130, v42, v46 op_sel:[0,0,1]
	v_cvt_pk_fp8_f32 v131, v58, v62 op_sel:[0,0,1]
	s_nop 0
	global_store_dwordx4 v161, v[128:131], s[20:21] offset:2048
	v_mul_f32_e32 v3, 0x42000000, v3
	v_mul_f32_e32 v7, 0x42000000, v7
	v_mul_f32_e32 v11, 0x42000000, v11
	v_mul_f32_e32 v15, 0x42000000, v15
	v_mul_f32_e32 v19, 0x42000000, v19
	v_mul_f32_e32 v23, 0x42000000, v23
	v_mul_f32_e32 v27, 0x42000000, v27
	v_mul_f32_e32 v31, 0x42000000, v31
	v_mul_f32_e32 v35, 0x42000000, v35
	v_mul_f32_e32 v39, 0x42000000, v39
	v_mul_f32_e32 v43, 0x42000000, v43
	v_mul_f32_e32 v47, 0x42000000, v47
	v_mul_f32_e32 v51, 0x42000000, v51
	v_mul_f32_e32 v55, 0x42000000, v55
	v_mul_f32_e32 v59, 0x42000000, v59
	v_mul_f32_e32 v63, 0x42000000, v63
	v_med3_f32 v3, v3, s28, v162
	v_med3_f32 v7, v7, s28, v162
	v_med3_f32 v11, v11, s28, v162
	v_med3_f32 v15, v15, s28, v162
	v_med3_f32 v19, v19, s28, v162
	v_med3_f32 v23, v23, s28, v162
	v_med3_f32 v27, v27, s28, v162
	v_med3_f32 v31, v31, s28, v162
	v_med3_f32 v35, v35, s28, v162
	v_med3_f32 v39, v39, s28, v162
	v_med3_f32 v43, v43, s28, v162
	v_med3_f32 v47, v47, s28, v162
	v_med3_f32 v51, v51, s28, v162
	v_med3_f32 v55, v55, s28, v162
	v_med3_f32 v59, v59, s28, v162
	v_med3_f32 v63, v63, s28, v162
	v_cvt_pk_fp8_f32 v136, v3, v7
	v_cvt_pk_fp8_f32 v137, v19, v23
	v_cvt_pk_fp8_f32 v138, v35, v39
	v_cvt_pk_fp8_f32 v139, v51, v55
	v_cvt_pk_fp8_f32 v136, v11, v15 op_sel:[0,0,1]
	v_cvt_pk_fp8_f32 v137, v27, v31 op_sel:[0,0,1]
	v_cvt_pk_fp8_f32 v138, v43, v47 op_sel:[0,0,1]
	v_cvt_pk_fp8_f32 v139, v59, v63 op_sel:[0,0,1]
	s_nop 0
	global_store_dwordx4 v161, v[136:139], s[20:21] offset:3072
	s_cmp_ge_u32 s7, s6
	s_cbranch_scc1 .Ltf7_done
	s_mov_b32 s4, s7
.Ltf7_loop:
	s_add_i32 s7, s4, s5
	s_cmp_lt_u32 s7, s6
	s_cbranch_scc0 .Ltf7_B_last
	s_lshr_b32 s22, s7, 8
	s_and_b32 s23, s7, 0xff
	s_mov_b64 s[16:17], s[12:13]
	s_add_i32 s22, s22, 56
	s_lshl_b32 s24, s22, 22
	s_lshr_b32 s25, s23, 5
	s_lshl_b32 s25, s25, 19
	s_and_b32 s26, s23, 31
	s_lshl_b32 s26, s26, 7
	s_add_i32 s24, s24, s25
	s_add_i32 s24, s24, s26
	s_add_u32 s16, s16, s24
	s_addc_u32 s17, s17, 0
	s_nop 0
	global_load_dwordx4 v[0:3], v144, s[16:17] nt
	global_load_dwordx4 v[4:7], v145, s[16:17] nt
	global_load_dwordx4 v[8:11], v146, s[16:17] nt
	global_load_dwordx4 v[12:15], v147, s[16:17] nt
	global_load_dwordx4 v[16:19], v148, s[16:17] nt
	global_load_dwordx4 v[20:23], v149, s[16:17] nt
	global_load_dwordx4 v[24:27], v150, s[16:17] nt
	global_load_dwordx4 v[28:31], v151, s[16:17] nt
	global_load_dwordx4 v[32:35], v152, s[16:17] nt
	global_load_dwordx4 v[36:39], v153, s[16:17] nt
	global_load_dwordx4 v[40:43], v154, s[16:17] nt
	global_load_dwordx4 v[44:47], v155, s[16:17] nt
	global_load_dwordx4 v[48:51], v156, s[16:17] nt
	global_load_dwordx4 v[52:55], v157, s[16:17] nt
	global_load_dwordx4 v[56:59], v158, s[16:17] nt
	global_load_dwordx4 v[60:63], v159, s[16:17] nt
	s_waitcnt vmcnt(20)
	s_branch .Ltf7_B_st

.Ltf7_B_st:
	s_lshr_b32 s22, s4, 8
	s_and_b32 s23, s4, 0xff
	s_add_i32 s22, s22, 56
	s_mul_i32 s24, s22, 0x300000
	s_lshr_b32 s25, s23, 5
	s_lshl_b32 s25, s25, 7
	s_add_i32 s24, s24, s25
	s_and_b32 s26, s23, 31
	s_lshr_b32 s25, s26, 3
	s_lshl_b32 s25, s25, 18
	s_add_i32 s24, s24, s25
	s_bfe_u32 s25, s26, 0x20001
	s_lshl_b32 s25, s25, 15
	s_add_i32 s24, s24, s25
	s_and_b32 s25, s26, 1
	s_lshl_b32 s25, s25, 14
	s_add_i32 s24, s24, s25
	s_add_u32 s20, s10, s24
	s_addc_u32 s21, s11, 0
	v_mul_f32_e32 v64, 0x42000000, v64
	v_mul_f32_e32 v68, 0x42000000, v68
	v_mul_f32_e32 v72, 0x42000000, v72
	v_mul_f32_e32 v76, 0x42000000, v76
	v_mul_f32_e32 v80, 0x42000000, v80
	v_mul_f32_e32 v84, 0x42000000, v84
	v_mul_f32_e32 v88, 0x42000000, v88
	v_mul_f32_e32 v92, 0x42000000, v92
	v_mul_f32_e32 v96, 0x42000000, v96
	v_mul_f32_e32 v100, 0x42000000, v100
	v_mul_f32_e32 v104, 0x42000000, v104
	v_mul_f32_e32 v108, 0x42000000, v108
	v_mul_f32_e32 v112, 0x42000000, v112
	v_mul_f32_e32 v116, 0x42000000, v116
	v_mul_f32_e32 v120, 0x42000000, v120
	v_mul_f32_e32 v124, 0x42000000, v124
	v_med3_f32 v64, v64, s28, v162
	v_med3_f32 v68, v68, s28, v162
	v_med3_f32 v72, v72, s28, v162
	v_med3_f32 v76, v76, s28, v162
	v_med3_f32 v80, v80, s28, v162
	v_med3_f32 v84, v84, s28, v162
	v_med3_f32 v88, v88, s28, v162
	v_med3_f32 v92, v92, s28, v162
	v_med3_f32 v96, v96, s28, v162
	v_med3_f32 v100, v100, s28, v162
	v_med3_f32 v104, v104, s28, v162
	v_med3_f32 v108, v108, s28, v162
	v_med3_f32 v112, v112, s28, v162
	v_med3_f32 v116, v116, s28, v162
	v_med3_f32 v120, v120, s28, v162
	v_med3_f32 v124, v124, s28, v162
	v_cvt_pk_fp8_f32 v128, v64, v68
	v_cvt_pk_fp8_f32 v129, v80, v84
	v_cvt_pk_fp8_f32 v130, v96, v100
	v_cvt_pk_fp8_f32 v131, v112, v116
	v_cvt_pk_fp8_f32 v128, v72, v76 op_sel:[0,0,1]
	v_cvt_pk_fp8_f32 v129, v88, v92 op_sel:[0,0,1]
	v_cvt_pk_fp8_f32 v130, v104, v108 op_sel:[0,0,1]
	v_cvt_pk_fp8_f32 v131, v120, v124 op_sel:[0,0,1]
	s_nop 0
	global_store_dwordx4 v161, v[128:131], s[20:21]
	v_mul_f32_e32 v65, 0x42000000, v65
	v_mul_f32_e32 v69, 0x42000000, v69
	v_mul_f32_e32 v73, 0x42000000, v73
	v_mul_f32_e32 v77, 0x42000000, v77
	v_mul_f32_e32 v81, 0x42000000, v81
	v_mul_f32_e32 v85, 0x42000000, v85
	v_mul_f32_e32 v89, 0x42000000, v89
	v_mul_f32_e32 v93, 0x42000000, v93
	v_mul_f32_e32 v97, 0x42000000, v97
	v_mul_f32_e32 v101, 0x42000000, v101
	v_mul_f32_e32 v105, 0x42000000, v105
	v_mul_f32_e32 v109, 0x42000000, v109
	v_mul_f32_e32 v113, 0x42000000, v113
	v_mul_f32_e32 v117, 0x42000000, v117
	v_mul_f32_e32 v121, 0x42000000, v121
	v_mul_f32_e32 v125, 0x42000000, v125
	v_med3_f32 v65, v65, s28, v162
	v_med3_f32 v69, v69, s28, v162
	v_med3_f32 v73, v73, s28, v162
	v_med3_f32 v77, v77, s28, v162
	v_med3_f32 v81, v81, s28, v162
	v_med3_f32 v85, v85, s28, v162
	v_med3_f32 v89, v89, s28, v162
	v_med3_f32 v93, v93, s28, v162
	v_med3_f32 v97, v97, s28, v162
	v_med3_f32 v101, v101, s28, v162
	v_med3_f32 v105, v105, s28, v162
	v_med3_f32 v109, v109, s28, v162
	v_med3_f32 v113, v113, s28, v162
	v_med3_f32 v117, v117, s28, v162
	v_med3_f32 v121, v121, s28, v162
	v_med3_f32 v125, v125, s28, v162
	v_cvt_pk_fp8_f32 v136, v65, v69
	v_cvt_pk_fp8_f32 v137, v81, v85
	v_cvt_pk_fp8_f32 v138, v97, v101
	v_cvt_pk_fp8_f32 v139, v113, v117
	v_cvt_pk_fp8_f32 v136, v73, v77 op_sel:[0,0,1]
	v_cvt_pk_fp8_f32 v137, v89, v93 op_sel:[0,0,1]
	v_cvt_pk_fp8_f32 v138, v105, v109 op_sel:[0,0,1]
	v_cvt_pk_fp8_f32 v139, v121, v125 op_sel:[0,0,1]
	s_nop 0
	global_store_dwordx4 v161, v[136:139], s[20:21] offset:1024
	v_mul_f32_e32 v66, 0x42000000, v66
	v_mul_f32_e32 v70, 0x42000000, v70
	v_mul_f32_e32 v74, 0x42000000, v74
	v_mul_f32_e32 v78, 0x42000000, v78
	v_mul_f32_e32 v82, 0x42000000, v82
	v_mul_f32_e32 v86, 0x42000000, v86
	v_mul_f32_e32 v90, 0x42000000, v90
	v_mul_f32_e32 v94, 0x42000000, v94
	v_mul_f32_e32 v98, 0x42000000, v98
	v_mul_f32_e32 v102, 0x42000000, v102
	v_mul_f32_e32 v106, 0x42000000, v106
	v_mul_f32_e32 v110, 0x42000000, v110
	v_mul_f32_e32 v114, 0x42000000, v114
	v_mul_f32_e32 v118, 0x42000000, v118
	v_mul_f32_e32 v122, 0x42000000, v122
	v_mul_f32_e32 v126, 0x42000000, v126
	v_med3_f32 v66, v66, s28, v162
	v_med3_f32 v70, v70, s28, v162
	v_med3_f32 v74, v74, s28, v162
	v_med3_f32 v78, v78, s28, v162
	v_med3_f32 v82, v82, s28, v162
	v_med3_f32 v86, v86, s28, v162
	v_med3_f32 v90, v90, s28, v162
	v_med3_f32 v94, v94, s28, v162
	v_med3_f32 v98, v98, s28, v162
	v_med3_f32 v102, v102, s28, v162
	v_med3_f32 v106, v106, s28, v162
	v_med3_f32 v110, v110, s28, v162
	v_med3_f32 v114, v114, s28, v162
	v_med3_f32 v118, v118, s28, v162
	v_med3_f32 v122, v122, s28, v162
	v_med3_f32 v126, v126, s28, v162
	v_cvt_pk_fp8_f32 v128, v66, v70
	v_cvt_pk_fp8_f32 v129, v82, v86
	v_cvt_pk_fp8_f32 v130, v98, v102
	v_cvt_pk_fp8_f32 v131, v114, v118
	v_cvt_pk_fp8_f32 v128, v74, v78 op_sel:[0,0,1]
	v_cvt_pk_fp8_f32 v129, v90, v94 op_sel:[0,0,1]
	v_cvt_pk_fp8_f32 v130, v106, v110 op_sel:[0,0,1]
	v_cvt_pk_fp8_f32 v131, v122, v126 op_sel:[0,0,1]
	s_nop 0
	global_store_dwordx4 v161, v[128:131], s[20:21] offset:2048
	v_mul_f32_e32 v67, 0x42000000, v67
	v_mul_f32_e32 v71, 0x42000000, v71
	v_mul_f32_e32 v75, 0x42000000, v75
	v_mul_f32_e32 v79, 0x42000000, v79
	v_mul_f32_e32 v83, 0x42000000, v83
	v_mul_f32_e32 v87, 0x42000000, v87
	v_mul_f32_e32 v91, 0x42000000, v91
	v_mul_f32_e32 v95, 0x42000000, v95
	v_mul_f32_e32 v99, 0x42000000, v99
	v_mul_f32_e32 v103, 0x42000000, v103
	v_mul_f32_e32 v107, 0x42000000, v107
	v_mul_f32_e32 v111, 0x42000000, v111
	v_mul_f32_e32 v115, 0x42000000, v115
	v_mul_f32_e32 v119, 0x42000000, v119
	v_mul_f32_e32 v123, 0x42000000, v123
	v_mul_f32_e32 v127, 0x42000000, v127
	v_med3_f32 v67, v67, s28, v162
	v_med3_f32 v71, v71, s28, v162
	v_med3_f32 v75, v75, s28, v162
	v_med3_f32 v79, v79, s28, v162
	v_med3_f32 v83, v83, s28, v162
	v_med3_f32 v87, v87, s28, v162
	v_med3_f32 v91, v91, s28, v162
	v_med3_f32 v95, v95, s28, v162
	v_med3_f32 v99, v99, s28, v162
	v_med3_f32 v103, v103, s28, v162
	v_med3_f32 v107, v107, s28, v162
	v_med3_f32 v111, v111, s28, v162
	v_med3_f32 v115, v115, s28, v162
	v_med3_f32 v119, v119, s28, v162
	v_med3_f32 v123, v123, s28, v162
	v_med3_f32 v127, v127, s28, v162
	v_cvt_pk_fp8_f32 v136, v67, v71
	v_cvt_pk_fp8_f32 v137, v83, v87
	v_cvt_pk_fp8_f32 v138, v99, v103
	v_cvt_pk_fp8_f32 v139, v115, v119
	v_cvt_pk_fp8_f32 v136, v75, v79 op_sel:[0,0,1]
	v_cvt_pk_fp8_f32 v137, v91, v95 op_sel:[0,0,1]
	v_cvt_pk_fp8_f32 v138, v107, v111 op_sel:[0,0,1]
	v_cvt_pk_fp8_f32 v139, v123, v127 op_sel:[0,0,1]
	s_nop 0
	global_store_dwordx4 v161, v[136:139], s[20:21] offset:3072
	s_cmp_ge_u32 s7, s6
	s_cbranch_scc1 .Ltf7_done
	s_mov_b32 s4, s7
	s_add_i32 s7, s4, s5
	s_cmp_lt_u32 s7, s6
	s_cbranch_scc0 .Ltf7_A_last
	s_lshr_b32 s22, s7, 8
	s_and_b32 s23, s7, 0xff
	s_mov_b64 s[16:17], s[12:13]
	s_add_i32 s22, s22, 56
	s_lshl_b32 s24, s22, 22
	s_lshr_b32 s25, s23, 5
	s_lshl_b32 s25, s25, 19
	s_and_b32 s26, s23, 31
	s_lshl_b32 s26, s26, 7
	s_add_i32 s24, s24, s25
	s_add_i32 s24, s24, s26
	s_add_u32 s16, s16, s24
	s_addc_u32 s17, s17, 0
	s_nop 0
	global_load_dwordx4 v[64:67], v144, s[16:17] nt
	global_load_dwordx4 v[68:71], v145, s[16:17] nt
	global_load_dwordx4 v[72:75], v146, s[16:17] nt
	global_load_dwordx4 v[76:79], v147, s[16:17] nt
	global_load_dwordx4 v[80:83], v148, s[16:17] nt
	global_load_dwordx4 v[84:87], v149, s[16:17] nt
	global_load_dwordx4 v[88:91], v150, s[16:17] nt
	global_load_dwordx4 v[92:95], v151, s[16:17] nt
	global_load_dwordx4 v[96:99], v152, s[16:17] nt
	global_load_dwordx4 v[100:103], v153, s[16:17] nt
	global_load_dwordx4 v[104:107], v154, s[16:17] nt
	global_load_dwordx4 v[108:111], v155, s[16:17] nt
	global_load_dwordx4 v[112:115], v156, s[16:17] nt
	global_load_dwordx4 v[116:119], v157, s[16:17] nt
	global_load_dwordx4 v[120:123], v158, s[16:17] nt
	global_load_dwordx4 v[124:127], v159, s[16:17] nt
	s_waitcnt vmcnt(20)
	s_branch .Ltf7_A_st

.Ltf7_A_st:
	s_lshr_b32 s22, s4, 8
	s_and_b32 s23, s4, 0xff
	s_add_i32 s22, s22, 56
	s_mul_i32 s24, s22, 0x300000
	s_lshr_b32 s25, s23, 5
	s_lshl_b32 s25, s25, 7
	s_add_i32 s24, s24, s25
	s_and_b32 s26, s23, 31
	s_lshr_b32 s25, s26, 3
	s_lshl_b32 s25, s25, 18
	s_add_i32 s24, s24, s25
	s_bfe_u32 s25, s26, 0x20001
	s_lshl_b32 s25, s25, 15
	s_add_i32 s24, s24, s25
	s_and_b32 s25, s26, 1
	s_lshl_b32 s25, s25, 14
	s_add_i32 s24, s24, s25
	s_add_u32 s20, s10, s24
	s_addc_u32 s21, s11, 0
	v_mul_f32_e32 v0, 0x42000000, v0
	v_mul_f32_e32 v4, 0x42000000, v4
	v_mul_f32_e32 v8, 0x42000000, v8
	v_mul_f32_e32 v12, 0x42000000, v12
	v_mul_f32_e32 v16, 0x42000000, v16
	v_mul_f32_e32 v20, 0x42000000, v20
	v_mul_f32_e32 v24, 0x42000000, v24
	v_mul_f32_e32 v28, 0x42000000, v28
	v_mul_f32_e32 v32, 0x42000000, v32
	v_mul_f32_e32 v36, 0x42000000, v36
	v_mul_f32_e32 v40, 0x42000000, v40
	v_mul_f32_e32 v44, 0x42000000, v44
	v_mul_f32_e32 v48, 0x42000000, v48
	v_mul_f32_e32 v52, 0x42000000, v52
	v_mul_f32_e32 v56, 0x42000000, v56
	v_mul_f32_e32 v60, 0x42000000, v60
	v_med3_f32 v0, v0, s28, v162
	v_med3_f32 v4, v4, s28, v162
	v_med3_f32 v8, v8, s28, v162
	v_med3_f32 v12, v12, s28, v162
	v_med3_f32 v16, v16, s28, v162
	v_med3_f32 v20, v20, s28, v162
	v_med3_f32 v24, v24, s28, v162
	v_med3_f32 v28, v28, s28, v162
	v_med3_f32 v32, v32, s28, v162
	v_med3_f32 v36, v36, s28, v162
	v_med3_f32 v40, v40, s28, v162
	v_med3_f32 v44, v44, s28, v162
	v_med3_f32 v48, v48, s28, v162
	v_med3_f32 v52, v52, s28, v162
	v_med3_f32 v56, v56, s28, v162
	v_med3_f32 v60, v60, s28, v162
	v_cvt_pk_fp8_f32 v128, v0, v4
	v_cvt_pk_fp8_f32 v129, v16, v20
	v_cvt_pk_fp8_f32 v130, v32, v36
	v_cvt_pk_fp8_f32 v131, v48, v52
	v_cvt_pk_fp8_f32 v128, v8, v12 op_sel:[0,0,1]
	v_cvt_pk_fp8_f32 v129, v24, v28 op_sel:[0,0,1]
	v_cvt_pk_fp8_f32 v130, v40, v44 op_sel:[0,0,1]
	v_cvt_pk_fp8_f32 v131, v56, v60 op_sel:[0,0,1]
	s_nop 0
	global_store_dwordx4 v161, v[128:131], s[20:21]
	v_mul_f32_e32 v1, 0x42000000, v1
	v_mul_f32_e32 v5, 0x42000000, v5
	v_mul_f32_e32 v9, 0x42000000, v9
	v_mul_f32_e32 v13, 0x42000000, v13
	v_mul_f32_e32 v17, 0x42000000, v17
	v_mul_f32_e32 v21, 0x42000000, v21
	v_mul_f32_e32 v25, 0x42000000, v25
	v_mul_f32_e32 v29, 0x42000000, v29
	v_mul_f32_e32 v33, 0x42000000, v33
	v_mul_f32_e32 v37, 0x42000000, v37
	v_mul_f32_e32 v41, 0x42000000, v41
	v_mul_f32_e32 v45, 0x42000000, v45
	v_mul_f32_e32 v49, 0x42000000, v49
	v_mul_f32_e32 v53, 0x42000000, v53
	v_mul_f32_e32 v57, 0x42000000, v57
	v_mul_f32_e32 v61, 0x42000000, v61
	v_med3_f32 v1, v1, s28, v162
	v_med3_f32 v5, v5, s28, v162
	v_med3_f32 v9, v9, s28, v162
	v_med3_f32 v13, v13, s28, v162
	v_med3_f32 v17, v17, s28, v162
	v_med3_f32 v21, v21, s28, v162
	v_med3_f32 v25, v25, s28, v162
	v_med3_f32 v29, v29, s28, v162
	v_med3_f32 v33, v33, s28, v162
	v_med3_f32 v37, v37, s28, v162
	v_med3_f32 v41, v41, s28, v162
	v_med3_f32 v45, v45, s28, v162
	v_med3_f32 v49, v49, s28, v162
	v_med3_f32 v53, v53, s28, v162
	v_med3_f32 v57, v57, s28, v162
	v_med3_f32 v61, v61, s28, v162
	v_cvt_pk_fp8_f32 v136, v1, v5
	v_cvt_pk_fp8_f32 v137, v17, v21
	v_cvt_pk_fp8_f32 v138, v33, v37
	v_cvt_pk_fp8_f32 v139, v49, v53
	v_cvt_pk_fp8_f32 v136, v9, v13 op_sel:[0,0,1]
	v_cvt_pk_fp8_f32 v137, v25, v29 op_sel:[0,0,1]
	v_cvt_pk_fp8_f32 v138, v41, v45 op_sel:[0,0,1]
	v_cvt_pk_fp8_f32 v139, v57, v61 op_sel:[0,0,1]
	s_nop 0
	global_store_dwordx4 v161, v[136:139], s[20:21] offset:1024
	v_mul_f32_e32 v2, 0x42000000, v2
	v_mul_f32_e32 v6, 0x42000000, v6
	v_mul_f32_e32 v10, 0x42000000, v10
	v_mul_f32_e32 v14, 0x42000000, v14
	v_mul_f32_e32 v18, 0x42000000, v18
	v_mul_f32_e32 v22, 0x42000000, v22
	v_mul_f32_e32 v26, 0x42000000, v26
	v_mul_f32_e32 v30, 0x42000000, v30
	v_mul_f32_e32 v34, 0x42000000, v34
	v_mul_f32_e32 v38, 0x42000000, v38
	v_mul_f32_e32 v42, 0x42000000, v42
	v_mul_f32_e32 v46, 0x42000000, v46
	v_mul_f32_e32 v50, 0x42000000, v50
	v_mul_f32_e32 v54, 0x42000000, v54
	v_mul_f32_e32 v58, 0x42000000, v58
	v_mul_f32_e32 v62, 0x42000000, v62
	v_med3_f32 v2, v2, s28, v162
	v_med3_f32 v6, v6, s28, v162
	v_med3_f32 v10, v10, s28, v162
	v_med3_f32 v14, v14, s28, v162
	v_med3_f32 v18, v18, s28, v162
	v_med3_f32 v22, v22, s28, v162
	v_med3_f32 v26, v26, s28, v162
	v_med3_f32 v30, v30, s28, v162
	v_med3_f32 v34, v34, s28, v162
	v_med3_f32 v38, v38, s28, v162
	v_med3_f32 v42, v42, s28, v162
	v_med3_f32 v46, v46, s28, v162
	v_med3_f32 v50, v50, s28, v162
	v_med3_f32 v54, v54, s28, v162
	v_med3_f32 v58, v58, s28, v162
	v_med3_f32 v62, v62, s28, v162
	v_cvt_pk_fp8_f32 v128, v2, v6
	v_cvt_pk_fp8_f32 v129, v18, v22
	v_cvt_pk_fp8_f32 v130, v34, v38
	v_cvt_pk_fp8_f32 v131, v50, v54
	v_cvt_pk_fp8_f32 v128, v10, v14 op_sel:[0,0,1]
	v_cvt_pk_fp8_f32 v129, v26, v30 op_sel:[0,0,1]
	v_cvt_pk_fp8_f32 v130, v42, v46 op_sel:[0,0,1]
	v_cvt_pk_fp8_f32 v131, v58, v62 op_sel:[0,0,1]
	s_nop 0
	global_store_dwordx4 v161, v[128:131], s[20:21] offset:2048
	v_mul_f32_e32 v3, 0x42000000, v3
	v_mul_f32_e32 v7, 0x42000000, v7
	v_mul_f32_e32 v11, 0x42000000, v11
	v_mul_f32_e32 v15, 0x42000000, v15
	v_mul_f32_e32 v19, 0x42000000, v19
	v_mul_f32_e32 v23, 0x42000000, v23
	v_mul_f32_e32 v27, 0x42000000, v27
	v_mul_f32_e32 v31, 0x42000000, v31
	v_mul_f32_e32 v35, 0x42000000, v35
	v_mul_f32_e32 v39, 0x42000000, v39
	v_mul_f32_e32 v43, 0x42000000, v43
	v_mul_f32_e32 v47, 0x42000000, v47
	v_mul_f32_e32 v51, 0x42000000, v51
	v_mul_f32_e32 v55, 0x42000000, v55
	v_mul_f32_e32 v59, 0x42000000, v59
	v_mul_f32_e32 v63, 0x42000000, v63
	v_med3_f32 v3, v3, s28, v162
	v_med3_f32 v7, v7, s28, v162
	v_med3_f32 v11, v11, s28, v162
	v_med3_f32 v15, v15, s28, v162
	v_med3_f32 v19, v19, s28, v162
	v_med3_f32 v23, v23, s28, v162
	v_med3_f32 v27, v27, s28, v162
	v_med3_f32 v31, v31, s28, v162
	v_med3_f32 v35, v35, s28, v162
	v_med3_f32 v39, v39, s28, v162
	v_med3_f32 v43, v43, s28, v162
	v_med3_f32 v47, v47, s28, v162
	v_med3_f32 v51, v51, s28, v162
	v_med3_f32 v55, v55, s28, v162
	v_med3_f32 v59, v59, s28, v162
	v_med3_f32 v63, v63, s28, v162
	v_cvt_pk_fp8_f32 v136, v3, v7
	v_cvt_pk_fp8_f32 v137, v19, v23
	v_cvt_pk_fp8_f32 v138, v35, v39
	v_cvt_pk_fp8_f32 v139, v51, v55
	v_cvt_pk_fp8_f32 v136, v11, v15 op_sel:[0,0,1]
	v_cvt_pk_fp8_f32 v137, v27, v31 op_sel:[0,0,1]
	v_cvt_pk_fp8_f32 v138, v43, v47 op_sel:[0,0,1]
	v_cvt_pk_fp8_f32 v139, v59, v63 op_sel:[0,0,1]
	s_nop 0
	global_store_dwordx4 v161, v[136:139], s[20:21] offset:3072
	s_cmp_ge_u32 s7, s6
	s_cbranch_scc1 .Ltf7_done
	s_mov_b32 s4, s7
	s_branch .Ltf7_loop
